# speedup vs baseline: 1.0030x; 1.0015x over previous
_Z11center_mainPKfPKcS0_Pf:
	s_load_dwordx4 s[4:7], s[0:1], 0x0
	s_load_dwordx4 s[8:11], s[0:1], 0x10
	s_and_b32 s3, s2, 7
	s_lshr_b32 s12, s2, 3
	s_mov_b32 s30, s2
	v_lshrrev_b32_e32 v1, 6, v0
	v_and_b32_e32 v2, 63, v0
	v_bfe_u32 v3, v0, 3, 3
	v_and_b32_e32 v4, 7, v0
	v_lshrrev_b32_e32 v5, 7, v0
	v_bfe_u32 v6, v0, 6, 1
	v_lshl_or_b32 v7, v5, 3, v3
	v_lshlrev_b32_e32 v8, 10, v7
	v_lshl_or_b32 v8, v6, 9, v8
	v_lshl_or_b32 v226, v4, 4, v8
	v_lshlrev_b32_e32 v17, 15, v1
	v_lshl_or_b32 v227, v2, 5, v17
	v_lshlrev_b32_e32 v237, 3, v0
	s_lshl_b32 s13, s3, 22
	s_lshl_b32 s14, s12, 15
	s_add_u32 s13, s13, s14
	s_lshl_b32 s15, s3, 18
	s_lshl_b32 s28, s3, 12
	s_waitcnt lgkmcnt(0)
	s_add_u32 s16, s4, s13
	s_addc_u32 s17, s5, 0
	global_load_dwordx4 v[194:197], v226, s[16:17] offset:0 nt
	global_load_dwordx4 v[198:201], v226, s[16:17] offset:128 nt
	global_load_dwordx4 v[202:205], v226, s[16:17] offset:256 nt
	global_load_dwordx4 v[206:209], v226, s[16:17] offset:384 nt
	s_add_u32 s8, s8, s28
	s_addc_u32 s9, s9, 0
	global_load_dwordx2 v[238:239], v237, s[8:9]
	s_add_u32 s24, s6, s15
	s_addc_u32 s25, s7, 0
	s_add_u32 s32, s24, 0x1000
	s_addc_u32 s33, s25, 0
	s_add_u32 s34, s24, 0x2000
	s_addc_u32 s35, s25, 0
	s_add_u32 s36, s24, 0x3000
	s_addc_u32 s37, s25, 0
	s_add_u32 s38, s24, 0x4000
	s_addc_u32 s39, s25, 0
	s_add_u32 s40, s24, 0x5000
	s_addc_u32 s41, s25, 0
	s_add_u32 s42, s24, 0x6000
	s_addc_u32 s43, s25, 0
	s_add_u32 s44, s24, 0x7000
	s_addc_u32 s45, s25, 0
	global_load_dwordx4 v[34:37], v227, s[24:25] offset:0
	global_load_dwordx4 v[38:41], v227, s[24:25] offset:16
	global_load_dwordx4 v[26:29], v227, s[24:25] offset:2048
	global_load_dwordx4 v[30:33], v227, s[24:25] offset:2064
	global_load_dwordx4 v[50:53], v227, s[32:33] offset:0
	global_load_dwordx4 v[54:57], v227, s[32:33] offset:16
	global_load_dwordx4 v[42:45], v227, s[32:33] offset:2048
	global_load_dwordx4 v[46:49], v227, s[32:33] offset:2064
	global_load_dwordx4 v[18:21], v227, s[34:35] offset:0
	global_load_dwordx4 v[22:25], v227, s[34:35] offset:16
	global_load_dwordx4 v[130:133], v227, s[34:35] offset:2048
	global_load_dwordx4 v[134:137], v227, s[34:35] offset:2064
	global_load_dwordx4 v[122:125], v227, s[36:37] offset:0
	global_load_dwordx4 v[126:129], v227, s[36:37] offset:16
	global_load_dwordx4 v[138:141], v227, s[36:37] offset:2048
	global_load_dwordx4 v[142:145], v227, s[36:37] offset:2064
	global_load_dwordx4 v[98:101], v227, s[38:39] offset:0
	global_load_dwordx4 v[102:105], v227, s[38:39] offset:16
	global_load_dwordx4 v[90:93], v227, s[38:39] offset:2048
	global_load_dwordx4 v[94:97], v227, s[38:39] offset:2064
	global_load_dwordx4 v[114:117], v227, s[40:41] offset:0
	global_load_dwordx4 v[118:121], v227, s[40:41] offset:16
	global_load_dwordx4 v[106:109], v227, s[40:41] offset:2048
	global_load_dwordx4 v[110:113], v227, s[40:41] offset:2064
	global_load_dwordx4 v[58:61], v227, s[42:43] offset:0
	global_load_dwordx4 v[62:65], v227, s[42:43] offset:16
	global_load_dwordx4 v[66:69], v227, s[42:43] offset:2048
	global_load_dwordx4 v[70:73], v227, s[42:43] offset:2064
	global_load_dwordx4 v[74:77], v227, s[44:45] offset:0
	global_load_dwordx4 v[78:81], v227, s[44:45] offset:16
	global_load_dwordx4 v[82:85], v227, s[44:45] offset:2048
	global_load_dwordx4 v[86:89], v227, s[44:45] offset:2064
	s_add_u32 s18, s16, 0x100000
	s_addc_u32 s19, s17, 0
	s_add_u32 s20, s16, 0x200000
	s_addc_u32 s21, s17, 0
	s_add_u32 s22, s16, 0x300000
	s_addc_u32 s23, s17, 0
	v_mul_u32_u24_e32 v9, 0x110, v7
	v_lshl_add_u32 v9, v6, 7, v9
	v_lshl_add_u32 v228, v4, 4, v9
	v_lshlrev_b32_e32 v10, 6, v7
	v_lshl_or_b32 v10, v6, 5, v10
	v_lshl_or_b32 v229, v4, 2, v10
	v_and_b32_e32 v11, 31, v0
	v_bfe_u32 v12, v0, 5, 1
	v_mul_u32_u24_e32 v13, 0x110, v11
	v_lshl_add_u32 v230, v12, 5, v13
	v_lshlrev_b32_e32 v14, 9, v1
	v_lshl_or_b32 v231, v12, 4, v14
	v_xor_b32_e32 v15, 32, v2
	v_lshlrev_b32_e32 v232, 2, v15
	v_xor_b32_e32 v15, 16, v2
	v_lshlrev_b32_e32 v247, 2, v15
	v_lshlrev_b32_e32 v16, 7, v1
	v_lshl_or_b32 v233, v11, 2, v16
	v_mov_b32_e32 v234, 0x7f7f7f7f
	s_waitcnt vmcnt(32)
	ds_write_b64 v237, v[238:239] offset:34816
	v_mul_f32_e32 v244, v194, v194
	v_mul_f32_e32 v245, v198, v198
	v_cvt_pk_fp8_f32 v240, v194, v195
	v_cvt_pk_fp8_f32 v241, v198, v199
	v_cvt_pk_fp8_f32 v242, v202, v203
	v_cvt_pk_fp8_f32 v243, v206, v207
	v_fmac_f32_e32 v244, v195, v195
	v_fmac_f32_e32 v245, v199, v199
	v_fmac_f32_e32 v244, v196, v196
	v_fmac_f32_e32 v245, v200, v200
	v_fmac_f32_e32 v244, v197, v197
	v_fmac_f32_e32 v245, v201, v201
	v_fmac_f32_e32 v244, v202, v202
	v_fmac_f32_e32 v245, v206, v206
	v_fmac_f32_e32 v244, v203, v203
	v_fmac_f32_e32 v245, v207, v207
	v_fmac_f32_e32 v244, v204, v204
	v_fmac_f32_e32 v245, v208, v208
	v_fmac_f32_e32 v244, v205, v205
	v_fmac_f32_e32 v245, v209, v209
	v_cvt_pk_fp8_f32 v240, v196, v197 op_sel:[0,0,1]
	v_cvt_pk_fp8_f32 v241, v200, v201 op_sel:[0,0,1]
	v_cvt_pk_fp8_f32 v242, v204, v205 op_sel:[0,0,1]
	v_cvt_pk_fp8_f32 v243, v208, v209 op_sel:[0,0,1]
	v_add_f32_e32 v244, v244, v245
	s_nop 0
	ds_write_b128 v228, v[240:243] offset:0
	ds_write_b32 v229, v244 offset:38912
	global_load_dwordx4 v[210:213], v226, s[18:19] offset:0 nt
	global_load_dwordx4 v[214:217], v226, s[18:19] offset:128 nt
	global_load_dwordx4 v[218:221], v226, s[18:19] offset:256 nt
	global_load_dwordx4 v[222:225], v226, s[18:19] offset:384 nt
	s_waitcnt lgkmcnt(0)
	s_barrier
	ds_read_b128 v[162:165], v230 offset:0
	ds_read_b128 v[166:169], v230 offset:16
	ds_read_b128 v[2:5], v231 offset:34816
	ds_read_b128 v[6:9], v231 offset:34848
	ds_read_b128 v[10:13], v231 offset:34880
	ds_read_b128 v[14:17], v231 offset:34912
	ds_read_b128 v[170:173], v230 offset:64
	ds_read_b128 v[174:177], v230 offset:80
	ds_read_b128 v[178:181], v230 offset:128
	ds_read_b128 v[182:185], v230 offset:144
	ds_read_b128 v[186:189], v230 offset:192
	ds_read_b128 v[190:193], v230 offset:208
	s_waitcnt vmcnt(34) lgkmcnt(6)
	v_mfma_scale_f32_32x32x64_f8f6f4 v[2:17], v[34:41], v[162:169], v[2:17], v234, v234 op_sel_hi:[0,0,0]
	s_waitcnt vmcnt(32) lgkmcnt(4)
	v_mfma_scale_f32_32x32x64_f8f6f4 v[2:17], v[26:33], v[170:177], v[2:17], v234, v234 op_sel_hi:[0,0,0]
	ds_read_b128 v[146:149], v231 offset:34944
	ds_read_b128 v[150:153], v231 offset:34976
	ds_read_b128 v[154:157], v231 offset:35008
	ds_read_b128 v[158:161], v231 offset:35040
	s_waitcnt vmcnt(30) lgkmcnt(6)
	v_mfma_scale_f32_32x32x64_f8f6f4 v[2:17], v[50:57], v[178:185], v[2:17], v234, v234 op_sel_hi:[0,0,0]
	s_waitcnt vmcnt(28) lgkmcnt(4)
	v_mfma_scale_f32_32x32x64_f8f6f4 v[2:17], v[42:49], v[186:193], v[2:17], v234, v234 op_sel_hi:[0,0,0]
	s_waitcnt lgkmcnt(0)
	s_waitcnt vmcnt(26)
	v_mfma_scale_f32_32x32x64_f8f6f4 v[146:161], v[18:25], v[162:169], v[146:161], v234, v234 op_sel_hi:[0,0,0]
	s_waitcnt vmcnt(24)
	v_mfma_scale_f32_32x32x64_f8f6f4 v[146:161], v[130:137], v[170:177], v[146:161], v234, v234 op_sel_hi:[0,0,0]
	v_min3_f32 v2, v2, v3, v4
	v_min3_f32 v5, v5, v6, v7
	v_min3_f32 v8, v8, v9, v10
	v_min3_f32 v11, v11, v12, v13
	v_min3_f32 v14, v14, v15, v16
	v_min3_f32 v2, v2, v5, v8
	v_min3_f32 v11, v11, v14, v17
	v_min_f32_e32 v235, v2, v11
	ds_read_b128 v[2:5], v231 offset:35072
	ds_read_b128 v[6:9], v231 offset:35104
	ds_read_b128 v[10:13], v231 offset:35136
	ds_read_b128 v[14:17], v231 offset:35168
	s_waitcnt vmcnt(22)
	v_mfma_scale_f32_32x32x64_f8f6f4 v[146:161], v[122:129], v[178:185], v[146:161], v234, v234 op_sel_hi:[0,0,0]
	s_waitcnt vmcnt(20)
	v_mfma_scale_f32_32x32x64_f8f6f4 v[146:161], v[138:145], v[186:193], v[146:161], v234, v234 op_sel_hi:[0,0,0]
	s_waitcnt vmcnt(18) lgkmcnt(0)
	v_mfma_scale_f32_32x32x64_f8f6f4 v[2:17], v[98:105], v[162:169], v[2:17], v234, v234 op_sel_hi:[0,0,0]
	s_waitcnt vmcnt(16)
	v_mfma_scale_f32_32x32x64_f8f6f4 v[2:17], v[90:97], v[170:177], v[2:17], v234, v234 op_sel_hi:[0,0,0]
	v_min3_f32 v146, v146, v147, v148
	v_min3_f32 v149, v149, v150, v151
	v_min3_f32 v152, v152, v153, v154
	v_min3_f32 v155, v155, v156, v157
	v_min3_f32 v158, v158, v159, v160
	v_min3_f32 v146, v146, v149, v152
	v_min3_f32 v155, v155, v158, v161
	v_min3_f32 v235, v235, v146, v155
	ds_read_b128 v[146:149], v231 offset:35200
	ds_read_b128 v[150:153], v231 offset:35232
	ds_read_b128 v[154:157], v231 offset:35264
	ds_read_b128 v[158:161], v231 offset:35296
	s_waitcnt vmcnt(14)
	v_mfma_scale_f32_32x32x64_f8f6f4 v[2:17], v[114:121], v[178:185], v[2:17], v234, v234 op_sel_hi:[0,0,0]
	s_waitcnt vmcnt(12)
	v_mfma_scale_f32_32x32x64_f8f6f4 v[2:17], v[106:113], v[186:193], v[2:17], v234, v234 op_sel_hi:[0,0,0]
	s_waitcnt vmcnt(10) lgkmcnt(0)
	v_mfma_scale_f32_32x32x64_f8f6f4 v[146:161], v[58:65], v[162:169], v[146:161], v234, v234 op_sel_hi:[0,0,0]
	s_waitcnt vmcnt(8)
	v_mfma_scale_f32_32x32x64_f8f6f4 v[146:161], v[66:73], v[170:177], v[146:161], v234, v234 op_sel_hi:[0,0,0]
	v_min3_f32 v2, v2, v3, v4
	v_min3_f32 v5, v5, v6, v7
	v_min3_f32 v8, v8, v9, v10
	v_min3_f32 v11, v11, v12, v13
	v_min3_f32 v14, v14, v15, v16
	v_min3_f32 v2, v2, v5, v8
	v_min3_f32 v11, v11, v14, v17
	v_min3_f32 v235, v235, v2, v11
	ds_read_b128 v[2:5], v231 offset:34816
	ds_read_b128 v[6:9], v231 offset:34848
	ds_read_b128 v[10:13], v231 offset:34880
	ds_read_b128 v[14:17], v231 offset:34912
	s_waitcnt vmcnt(6)
	v_mfma_scale_f32_32x32x64_f8f6f4 v[146:161], v[74:81], v[178:185], v[146:161], v234, v234 op_sel_hi:[0,0,0]
	s_waitcnt vmcnt(4)
	v_mfma_scale_f32_32x32x64_f8f6f4 v[146:161], v[82:89], v[186:193], v[146:161], v234, v234 op_sel_hi:[0,0,0]
	s_waitcnt vmcnt(0)
	v_mul_f32_e32 v244, v210, v210
	v_mul_f32_e32 v245, v214, v214
	v_cvt_pk_fp8_f32 v240, v210, v211
	v_cvt_pk_fp8_f32 v241, v214, v215
	v_cvt_pk_fp8_f32 v242, v218, v219
	v_cvt_pk_fp8_f32 v243, v222, v223
	v_fmac_f32_e32 v244, v211, v211
	v_fmac_f32_e32 v245, v215, v215
	v_fmac_f32_e32 v244, v212, v212
	v_fmac_f32_e32 v245, v216, v216
	v_fmac_f32_e32 v244, v213, v213
	v_fmac_f32_e32 v245, v217, v217
	v_fmac_f32_e32 v244, v218, v218
	v_fmac_f32_e32 v245, v222, v222
	v_fmac_f32_e32 v244, v219, v219
	v_fmac_f32_e32 v245, v223, v223
	v_fmac_f32_e32 v244, v220, v220
	v_fmac_f32_e32 v245, v224, v224
	v_fmac_f32_e32 v244, v221, v221
	v_fmac_f32_e32 v245, v225, v225
	v_cvt_pk_fp8_f32 v240, v212, v213 op_sel:[0,0,1]
	v_cvt_pk_fp8_f32 v241, v216, v217 op_sel:[0,0,1]
	v_cvt_pk_fp8_f32 v242, v220, v221 op_sel:[0,0,1]
	v_cvt_pk_fp8_f32 v243, v224, v225 op_sel:[0,0,1]
	v_add_f32_e32 v244, v244, v245
	s_nop 0
	ds_write_b128 v228, v[240:243] offset:8704
	ds_write_b32 v229, v244 offset:40960
	global_load_dwordx4 v[194:197], v226, s[20:21] offset:0 nt
	global_load_dwordx4 v[198:201], v226, s[20:21] offset:128 nt
	global_load_dwordx4 v[202:205], v226, s[20:21] offset:256 nt
	global_load_dwordx4 v[206:209], v226, s[20:21] offset:384 nt
	s_waitcnt lgkmcnt(0)
	s_barrier
	ds_read_b128 v[162:165], v230 offset:8704
	ds_read_b128 v[166:169], v230 offset:8720
	ds_read_b128 v[170:173], v230 offset:8768
	ds_read_b128 v[174:177], v230 offset:8784
	ds_read_b128 v[178:181], v230 offset:8832
	ds_read_b128 v[182:185], v230 offset:8848
	ds_read_b128 v[186:189], v230 offset:8896
	ds_read_b128 v[190:193], v230 offset:8912
	s_waitcnt lgkmcnt(6)
	v_mfma_scale_f32_32x32x64_f8f6f4 v[2:17], v[34:41], v[162:169], v[2:17], v234, v234 op_sel_hi:[0,0,0]
	s_waitcnt lgkmcnt(4)
	v_mfma_scale_f32_32x32x64_f8f6f4 v[2:17], v[26:33], v[170:177], v[2:17], v234, v234 op_sel_hi:[0,0,0]
	v_min3_f32 v146, v146, v147, v148
	v_min3_f32 v149, v149, v150, v151
	v_min3_f32 v152, v152, v153, v154
	v_min3_f32 v155, v155, v156, v157
	v_min3_f32 v158, v158, v159, v160
	v_min3_f32 v146, v146, v149, v152
	v_min3_f32 v155, v155, v158, v161
	v_min3_f32 v235, v235, v146, v155
	ds_bpermute_b32 v246, v232, v235
	ds_read_b128 v[146:149], v231 offset:34944
	ds_read_b128 v[150:153], v231 offset:34976
	ds_read_b128 v[154:157], v231 offset:35008
	ds_read_b128 v[158:161], v231 offset:35040
	s_waitcnt lgkmcnt(7)
	v_mfma_scale_f32_32x32x64_f8f6f4 v[2:17], v[50:57], v[178:185], v[2:17], v234, v234 op_sel_hi:[0,0,0]
	s_waitcnt lgkmcnt(5)
	v_mfma_scale_f32_32x32x64_f8f6f4 v[2:17], v[42:49], v[186:193], v[2:17], v234, v234 op_sel_hi:[0,0,0]
	s_waitcnt lgkmcnt(0)
	v_min_f32_e32 v246, v235, v246
	ds_write_b32 v233, v246 offset:47104
	v_mfma_scale_f32_32x32x64_f8f6f4 v[146:161], v[18:25], v[162:169], v[146:161], v234, v234 op_sel_hi:[0,0,0]
	v_mfma_scale_f32_32x32x64_f8f6f4 v[146:161], v[130:137], v[170:177], v[146:161], v234, v234 op_sel_hi:[0,0,0]
	v_min3_f32 v2, v2, v3, v4
	v_min3_f32 v5, v5, v6, v7
	v_min3_f32 v8, v8, v9, v10
	v_min3_f32 v11, v11, v12, v13
	v_min3_f32 v14, v14, v15, v16
	v_min3_f32 v2, v2, v5, v8
	v_min3_f32 v11, v11, v14, v17
	v_min_f32_e32 v236, v2, v11
	ds_read_b128 v[2:5], v231 offset:35072
	ds_read_b128 v[6:9], v231 offset:35104
	ds_read_b128 v[10:13], v231 offset:35136
	ds_read_b128 v[14:17], v231 offset:35168
	v_mfma_scale_f32_32x32x64_f8f6f4 v[146:161], v[122:129], v[178:185], v[146:161], v234, v234 op_sel_hi:[0,0,0]
	v_mfma_scale_f32_32x32x64_f8f6f4 v[146:161], v[138:145], v[186:193], v[146:161], v234, v234 op_sel_hi:[0,0,0]
	s_waitcnt lgkmcnt(0)
	v_mfma_scale_f32_32x32x64_f8f6f4 v[2:17], v[98:105], v[162:169], v[2:17], v234, v234 op_sel_hi:[0,0,0]
	v_mfma_scale_f32_32x32x64_f8f6f4 v[2:17], v[90:97], v[170:177], v[2:17], v234, v234 op_sel_hi:[0,0,0]
	v_min3_f32 v146, v146, v147, v148
	v_min3_f32 v149, v149, v150, v151
	v_min3_f32 v152, v152, v153, v154
	v_min3_f32 v155, v155, v156, v157
	v_min3_f32 v158, v158, v159, v160
	v_min3_f32 v146, v146, v149, v152
	v_min3_f32 v155, v155, v158, v161
	v_min3_f32 v236, v236, v146, v155
	ds_read_b128 v[146:149], v231 offset:35200
	ds_read_b128 v[150:153], v231 offset:35232
	ds_read_b128 v[154:157], v231 offset:35264
	ds_read_b128 v[158:161], v231 offset:35296
	v_mfma_scale_f32_32x32x64_f8f6f4 v[2:17], v[114:121], v[178:185], v[2:17], v234, v234 op_sel_hi:[0,0,0]
	v_mfma_scale_f32_32x32x64_f8f6f4 v[2:17], v[106:113], v[186:193], v[2:17], v234, v234 op_sel_hi:[0,0,0]
	s_waitcnt lgkmcnt(0)
	v_mfma_scale_f32_32x32x64_f8f6f4 v[146:161], v[58:65], v[162:169], v[146:161], v234, v234 op_sel_hi:[0,0,0]
	v_mfma_scale_f32_32x32x64_f8f6f4 v[146:161], v[66:73], v[170:177], v[146:161], v234, v234 op_sel_hi:[0,0,0]
	v_min3_f32 v2, v2, v3, v4
	v_min3_f32 v5, v5, v6, v7
	v_min3_f32 v8, v8, v9, v10
	v_min3_f32 v11, v11, v12, v13
	v_min3_f32 v14, v14, v15, v16
	v_min3_f32 v2, v2, v5, v8
	v_min3_f32 v11, v11, v14, v17
	v_min3_f32 v236, v236, v2, v11
	ds_read_b128 v[2:5], v231 offset:34816
	ds_read_b128 v[6:9], v231 offset:34848
	ds_read_b128 v[10:13], v231 offset:34880
	ds_read_b128 v[14:17], v231 offset:34912
	v_mfma_scale_f32_32x32x64_f8f6f4 v[146:161], v[74:81], v[178:185], v[146:161], v234, v234 op_sel_hi:[0,0,0]
	v_mfma_scale_f32_32x32x64_f8f6f4 v[146:161], v[82:89], v[186:193], v[146:161], v234, v234 op_sel_hi:[0,0,0]
	s_waitcnt vmcnt(0)
	v_mul_f32_e32 v244, v194, v194
	v_mul_f32_e32 v245, v198, v198
	v_cvt_pk_fp8_f32 v240, v194, v195
	v_cvt_pk_fp8_f32 v241, v198, v199
	v_cvt_pk_fp8_f32 v242, v202, v203
	v_cvt_pk_fp8_f32 v243, v206, v207
	v_fmac_f32_e32 v244, v195, v195
	v_fmac_f32_e32 v245, v199, v199
	v_fmac_f32_e32 v244, v196, v196
	v_fmac_f32_e32 v245, v200, v200
	v_fmac_f32_e32 v244, v197, v197
	v_fmac_f32_e32 v245, v201, v201
	v_fmac_f32_e32 v244, v202, v202
	v_fmac_f32_e32 v245, v206, v206
	v_fmac_f32_e32 v244, v203, v203
	v_fmac_f32_e32 v245, v207, v207
	v_fmac_f32_e32 v244, v204, v204
	v_fmac_f32_e32 v245, v208, v208
	v_fmac_f32_e32 v244, v205, v205
	v_fmac_f32_e32 v245, v209, v209
	v_cvt_pk_fp8_f32 v240, v196, v197 op_sel:[0,0,1]
	v_cvt_pk_fp8_f32 v241, v200, v201 op_sel:[0,0,1]
	v_cvt_pk_fp8_f32 v242, v204, v205 op_sel:[0,0,1]
	v_cvt_pk_fp8_f32 v243, v208, v209 op_sel:[0,0,1]
	v_add_f32_e32 v244, v244, v245
	s_nop 0
	ds_write_b128 v228, v[240:243] offset:17408
	ds_write_b32 v229, v244 offset:43008
	global_load_dwordx4 v[210:213], v226, s[22:23] offset:0 nt
	global_load_dwordx4 v[214:217], v226, s[22:23] offset:128 nt
	global_load_dwordx4 v[218:221], v226, s[22:23] offset:256 nt
	global_load_dwordx4 v[222:225], v226, s[22:23] offset:384 nt
	s_waitcnt lgkmcnt(0)
	s_barrier
	ds_read_b128 v[162:165], v230 offset:17408
	ds_read_b128 v[166:169], v230 offset:17424
	ds_read_b128 v[170:173], v230 offset:17472
	ds_read_b128 v[174:177], v230 offset:17488
	ds_read_b128 v[178:181], v230 offset:17536
	ds_read_b128 v[182:185], v230 offset:17552
	ds_read_b128 v[186:189], v230 offset:17600
	ds_read_b128 v[190:193], v230 offset:17616
	s_waitcnt lgkmcnt(6)
	v_mfma_scale_f32_32x32x64_f8f6f4 v[2:17], v[34:41], v[162:169], v[2:17], v234, v234 op_sel_hi:[0,0,0]
	s_waitcnt lgkmcnt(4)
	v_mfma_scale_f32_32x32x64_f8f6f4 v[2:17], v[26:33], v[170:177], v[2:17], v234, v234 op_sel_hi:[0,0,0]
	v_min3_f32 v146, v146, v147, v148
	v_min3_f32 v149, v149, v150, v151
	v_min3_f32 v152, v152, v153, v154
	v_min3_f32 v155, v155, v156, v157
	v_min3_f32 v158, v158, v159, v160
	v_min3_f32 v146, v146, v149, v152
	v_min3_f32 v155, v155, v158, v161
	v_min3_f32 v236, v236, v146, v155
	ds_bpermute_b32 v246, v232, v236
	ds_read_b128 v[146:149], v231 offset:34944
	ds_read_b128 v[150:153], v231 offset:34976
	ds_read_b128 v[154:157], v231 offset:35008
	ds_read_b128 v[158:161], v231 offset:35040
	s_waitcnt lgkmcnt(7)
	v_mfma_scale_f32_32x32x64_f8f6f4 v[2:17], v[50:57], v[178:185], v[2:17], v234, v234 op_sel_hi:[0,0,0]
	s_waitcnt lgkmcnt(5)
	v_mfma_scale_f32_32x32x64_f8f6f4 v[2:17], v[42:49], v[186:193], v[2:17], v234, v234 op_sel_hi:[0,0,0]
	s_waitcnt lgkmcnt(0)
	v_min_f32_e32 v246, v236, v246
	ds_write_b32 v233, v246 offset:48128
	v_mfma_scale_f32_32x32x64_f8f6f4 v[146:161], v[18:25], v[162:169], v[146:161], v234, v234 op_sel_hi:[0,0,0]
	v_mfma_scale_f32_32x32x64_f8f6f4 v[146:161], v[130:137], v[170:177], v[146:161], v234, v234 op_sel_hi:[0,0,0]
	v_min3_f32 v2, v2, v3, v4
	v_min3_f32 v5, v5, v6, v7
	v_min3_f32 v8, v8, v9, v10
	v_min3_f32 v11, v11, v12, v13
	v_min3_f32 v14, v14, v15, v16
	v_min3_f32 v2, v2, v5, v8
	v_min3_f32 v11, v11, v14, v17
	v_min_f32_e32 v235, v2, v11
	ds_read_b128 v[2:5], v231 offset:35072
	ds_read_b128 v[6:9], v231 offset:35104
	ds_read_b128 v[10:13], v231 offset:35136
	ds_read_b128 v[14:17], v231 offset:35168
	v_mfma_scale_f32_32x32x64_f8f6f4 v[146:161], v[122:129], v[178:185], v[146:161], v234, v234 op_sel_hi:[0,0,0]
	v_mfma_scale_f32_32x32x64_f8f6f4 v[146:161], v[138:145], v[186:193], v[146:161], v234, v234 op_sel_hi:[0,0,0]
	s_waitcnt lgkmcnt(0)
	v_mfma_scale_f32_32x32x64_f8f6f4 v[2:17], v[98:105], v[162:169], v[2:17], v234, v234 op_sel_hi:[0,0,0]
	v_mfma_scale_f32_32x32x64_f8f6f4 v[2:17], v[90:97], v[170:177], v[2:17], v234, v234 op_sel_hi:[0,0,0]
	v_min3_f32 v146, v146, v147, v148
	v_min3_f32 v149, v149, v150, v151
	v_min3_f32 v152, v152, v153, v154
	v_min3_f32 v155, v155, v156, v157
	v_min3_f32 v158, v158, v159, v160
	v_min3_f32 v146, v146, v149, v152
	v_min3_f32 v155, v155, v158, v161
	v_min3_f32 v235, v235, v146, v155
	ds_read_b128 v[146:149], v231 offset:35200
	ds_read_b128 v[150:153], v231 offset:35232
	ds_read_b128 v[154:157], v231 offset:35264
	ds_read_b128 v[158:161], v231 offset:35296
	v_mfma_scale_f32_32x32x64_f8f6f4 v[2:17], v[114:121], v[178:185], v[2:17], v234, v234 op_sel_hi:[0,0,0]
	v_mfma_scale_f32_32x32x64_f8f6f4 v[2:17], v[106:113], v[186:193], v[2:17], v234, v234 op_sel_hi:[0,0,0]
	s_waitcnt lgkmcnt(0)
	v_mfma_scale_f32_32x32x64_f8f6f4 v[146:161], v[58:65], v[162:169], v[146:161], v234, v234 op_sel_hi:[0,0,0]
	v_mfma_scale_f32_32x32x64_f8f6f4 v[146:161], v[66:73], v[170:177], v[146:161], v234, v234 op_sel_hi:[0,0,0]
	v_min3_f32 v2, v2, v3, v4
	v_min3_f32 v5, v5, v6, v7
	v_min3_f32 v8, v8, v9, v10
	v_min3_f32 v11, v11, v12, v13
	v_min3_f32 v14, v14, v15, v16
	v_min3_f32 v2, v2, v5, v8
	v_min3_f32 v11, v11, v14, v17
	v_min3_f32 v235, v235, v2, v11
	ds_read_b128 v[2:5], v231 offset:34816
	ds_read_b128 v[6:9], v231 offset:34848
	ds_read_b128 v[10:13], v231 offset:34880
	ds_read_b128 v[14:17], v231 offset:34912
	v_mfma_scale_f32_32x32x64_f8f6f4 v[146:161], v[74:81], v[178:185], v[146:161], v234, v234 op_sel_hi:[0,0,0]
	v_mfma_scale_f32_32x32x64_f8f6f4 v[146:161], v[82:89], v[186:193], v[146:161], v234, v234 op_sel_hi:[0,0,0]
	s_waitcnt vmcnt(0)
	v_mul_f32_e32 v244, v210, v210
	v_mul_f32_e32 v245, v214, v214
	v_cvt_pk_fp8_f32 v240, v210, v211
	v_cvt_pk_fp8_f32 v241, v214, v215
	v_cvt_pk_fp8_f32 v242, v218, v219
	v_cvt_pk_fp8_f32 v243, v222, v223
	v_fmac_f32_e32 v244, v211, v211
	v_fmac_f32_e32 v245, v215, v215
	v_fmac_f32_e32 v244, v212, v212
	v_fmac_f32_e32 v245, v216, v216
	v_fmac_f32_e32 v244, v213, v213
	v_fmac_f32_e32 v245, v217, v217
	v_fmac_f32_e32 v244, v218, v218
	v_fmac_f32_e32 v245, v222, v222
	v_fmac_f32_e32 v244, v219, v219
	v_fmac_f32_e32 v245, v223, v223
	v_fmac_f32_e32 v244, v220, v220
	v_fmac_f32_e32 v245, v224, v224
	v_fmac_f32_e32 v244, v221, v221
	v_fmac_f32_e32 v245, v225, v225
	v_cvt_pk_fp8_f32 v240, v212, v213 op_sel:[0,0,1]
	v_cvt_pk_fp8_f32 v241, v216, v217 op_sel:[0,0,1]
	v_cvt_pk_fp8_f32 v242, v220, v221 op_sel:[0,0,1]
	v_cvt_pk_fp8_f32 v243, v224, v225 op_sel:[0,0,1]
	v_add_f32_e32 v244, v244, v245
	s_nop 0
	ds_write_b128 v228, v[240:243] offset:26112
	ds_write_b32 v229, v244 offset:45056
	s_waitcnt lgkmcnt(0)
	s_barrier
	ds_read_b128 v[162:165], v230 offset:26112
	ds_read_b128 v[166:169], v230 offset:26128
	ds_read_b128 v[170:173], v230 offset:26176
	ds_read_b128 v[174:177], v230 offset:26192
	ds_read_b128 v[178:181], v230 offset:26240
	ds_read_b128 v[182:185], v230 offset:26256
	ds_read_b128 v[186:189], v230 offset:26304
	ds_read_b128 v[190:193], v230 offset:26320
	s_waitcnt lgkmcnt(6)
	v_mfma_scale_f32_32x32x64_f8f6f4 v[2:17], v[34:41], v[162:169], v[2:17], v234, v234 op_sel_hi:[0,0,0]
	s_waitcnt lgkmcnt(4)
	v_mfma_scale_f32_32x32x64_f8f6f4 v[2:17], v[26:33], v[170:177], v[2:17], v234, v234 op_sel_hi:[0,0,0]
	v_min3_f32 v146, v146, v147, v148
	v_min3_f32 v149, v149, v150, v151
	v_min3_f32 v152, v152, v153, v154
	v_min3_f32 v155, v155, v156, v157
	v_min3_f32 v158, v158, v159, v160
	v_min3_f32 v146, v146, v149, v152
	v_min3_f32 v155, v155, v158, v161
	v_min3_f32 v235, v235, v146, v155
	ds_bpermute_b32 v246, v232, v235
	ds_read_b128 v[146:149], v231 offset:34944
	ds_read_b128 v[150:153], v231 offset:34976
	ds_read_b128 v[154:157], v231 offset:35008
	ds_read_b128 v[158:161], v231 offset:35040
	s_waitcnt lgkmcnt(7)
	v_mfma_scale_f32_32x32x64_f8f6f4 v[2:17], v[50:57], v[178:185], v[2:17], v234, v234 op_sel_hi:[0,0,0]
	s_waitcnt lgkmcnt(5)
	v_mfma_scale_f32_32x32x64_f8f6f4 v[2:17], v[42:49], v[186:193], v[2:17], v234, v234 op_sel_hi:[0,0,0]
	s_waitcnt lgkmcnt(0)
	v_min_f32_e32 v246, v235, v246
	ds_write_b32 v233, v246 offset:49152
	v_mfma_scale_f32_32x32x64_f8f6f4 v[146:161], v[18:25], v[162:169], v[146:161], v234, v234 op_sel_hi:[0,0,0]
	v_mfma_scale_f32_32x32x64_f8f6f4 v[146:161], v[130:137], v[170:177], v[146:161], v234, v234 op_sel_hi:[0,0,0]
	v_min3_f32 v2, v2, v3, v4
	v_min3_f32 v5, v5, v6, v7
	v_min3_f32 v8, v8, v9, v10
	v_min3_f32 v11, v11, v12, v13
	v_min3_f32 v14, v14, v15, v16
	v_min3_f32 v2, v2, v5, v8
	v_min3_f32 v11, v11, v14, v17
	v_min_f32_e32 v236, v2, v11
	ds_read_b128 v[2:5], v231 offset:35072
	ds_read_b128 v[6:9], v231 offset:35104
	ds_read_b128 v[10:13], v231 offset:35136
	ds_read_b128 v[14:17], v231 offset:35168
	v_mfma_scale_f32_32x32x64_f8f6f4 v[146:161], v[122:129], v[178:185], v[146:161], v234, v234 op_sel_hi:[0,0,0]
	v_mfma_scale_f32_32x32x64_f8f6f4 v[146:161], v[138:145], v[186:193], v[146:161], v234, v234 op_sel_hi:[0,0,0]
	s_waitcnt lgkmcnt(0)
	v_mfma_scale_f32_32x32x64_f8f6f4 v[2:17], v[98:105], v[162:169], v[2:17], v234, v234 op_sel_hi:[0,0,0]
	v_mfma_scale_f32_32x32x64_f8f6f4 v[2:17], v[90:97], v[170:177], v[2:17], v234, v234 op_sel_hi:[0,0,0]
	v_min3_f32 v146, v146, v147, v148
	v_min3_f32 v149, v149, v150, v151
	v_min3_f32 v152, v152, v153, v154
	v_min3_f32 v155, v155, v156, v157
	v_min3_f32 v158, v158, v159, v160
	v_min3_f32 v146, v146, v149, v152
	v_min3_f32 v155, v155, v158, v161
	v_min3_f32 v236, v236, v146, v155
	ds_read_b128 v[146:149], v231 offset:35200
	ds_read_b128 v[150:153], v231 offset:35232
	ds_read_b128 v[154:157], v231 offset:35264
	ds_read_b128 v[158:161], v231 offset:35296
	v_mfma_scale_f32_32x32x64_f8f6f4 v[2:17], v[114:121], v[178:185], v[2:17], v234, v234 op_sel_hi:[0,0,0]
	v_mfma_scale_f32_32x32x64_f8f6f4 v[2:17], v[106:113], v[186:193], v[2:17], v234, v234 op_sel_hi:[0,0,0]
	s_waitcnt lgkmcnt(0)
	v_mfma_scale_f32_32x32x64_f8f6f4 v[146:161], v[58:65], v[162:169], v[146:161], v234, v234 op_sel_hi:[0,0,0]
	v_mfma_scale_f32_32x32x64_f8f6f4 v[146:161], v[66:73], v[170:177], v[146:161], v234, v234 op_sel_hi:[0,0,0]
	v_min3_f32 v2, v2, v3, v4
	v_min3_f32 v5, v5, v6, v7
	v_min3_f32 v8, v8, v9, v10
	v_min3_f32 v11, v11, v12, v13
	v_min3_f32 v14, v14, v15, v16
	v_min3_f32 v2, v2, v5, v8
	v_min3_f32 v11, v11, v14, v17
	v_min3_f32 v236, v236, v2, v11
	v_cmp_gt_u32_e32 vcc, 0x80, v0
	s_and_saveexec_b64 s[34:35], vcc
	v_lshlrev_b32_e32 v36, 6, v0
	ds_read_b128 v[20:23], v36 offset:38912
	ds_read_b128 v[24:27], v36 offset:38928
	ds_read_b128 v[28:31], v36 offset:38944
	ds_read_b128 v[32:35], v36 offset:38960
	s_mov_b64 exec, s[34:35]
	v_mfma_scale_f32_32x32x64_f8f6f4 v[146:161], v[74:81], v[178:185], v[146:161], v234, v234 op_sel_hi:[0,0,0]
	v_mfma_scale_f32_32x32x64_f8f6f4 v[146:161], v[82:89], v[186:193], v[146:161], v234, v234 op_sel_hi:[0,0,0]
	s_nop 15
	s_nop 3
	v_min3_f32 v146, v146, v147, v148
	v_min3_f32 v149, v149, v150, v151
	v_min3_f32 v152, v152, v153, v154
	v_min3_f32 v155, v155, v156, v157
	v_min3_f32 v158, v158, v159, v160
	v_min3_f32 v146, v146, v149, v152
	v_min3_f32 v155, v155, v158, v161
	v_min3_f32 v236, v236, v146, v155
	ds_bpermute_b32 v246, v232, v236
	s_waitcnt lgkmcnt(0)
	v_min_f32_e32 v246, v236, v246
	ds_write_b32 v233, v246 offset:50176
	s_waitcnt lgkmcnt(0)
	s_barrier
	v_readfirstlane_b32 s2, v1
	s_nop 3
	s_cmp_gt_u32 s2, 1
	s_cbranch_scc1 .Lmain_end
	v_and_b32_e32 v2, 31, v0
	v_lshlrev_b32_e32 v3, 5, v0
	v_and_b32_e32 v3, 0xc00, v3
	v_lshl_or_b32 v8, v2, 2, v3
	v_add_u32_e32 v8, 0xb800, v8
	ds_read2_b32 v[2:3], v8 offset1:32
	ds_read2_b32 v[4:5], v8 offset0:64 offset1:96
	ds_read2_b32 v[6:7], v8 offset0:128 offset1:160
	ds_read2_b32 v[10:11], v8 offset0:192 offset1:224
	s_mov_b32 s8, 0xf800000
	s_lshr_b32 s2, s30, 3
	s_lshl_b32 s2, s2, 7
	s_add_u32 s2, s2, 0x300000
	s_add_u32 s6, s6, s2
	s_addc_u32 s7, s7, 0
	s_mov_b32 s4, 0
	s_mov_b32 s5, 0x41d00000
	s_mov_b32 s16, 0
	s_mov_b32 s17, 0x420e0000
	s_waitcnt lgkmcnt(0)
	v_min3_f32 v2, v2, v3, v4
	v_min3_f32 v5, v5, v6, v7
	v_min3_f32 v2, v2, v10, v11
	v_min_f32_e32 v2, v2, v5
	s_waitcnt lgkmcnt(0)
	v_add_f32_e32 v20, v20, v21
	v_add_f32_e32 v22, v22, v23
	v_add_f32_e32 v24, v24, v25
	v_add_f32_e32 v26, v26, v27
	v_add_f32_e32 v28, v28, v29
	v_add_f32_e32 v30, v30, v31
	v_add_f32_e32 v32, v32, v33
	v_add_f32_e32 v34, v34, v35
	v_add_f32_e32 v20, v20, v22
	v_add_f32_e32 v24, v24, v26
	v_add_f32_e32 v28, v28, v30
	v_add_f32_e32 v32, v32, v34
	v_add_f32_e32 v20, v20, v24
	v_add_f32_e32 v28, v28, v32
	v_add_f32_e32 v20, v20, v28
	v_add_f32_e32 v2, v2, v20
	v_max_f32_e32 v2, 0, v2
	v_mul_f32_e32 v3, 0x4f800000, v2
	v_cmp_gt_f32_e32 vcc, s8, v2
	s_nop 1
	v_cndmask_b32_e32 v2, v2, v3, vcc
	v_sqrt_f32_e32 v3, v2
	s_nop 0
	v_add_u32_e32 v4, -1, v3
	v_fma_f32 v5, -v4, v3, v2
	v_cmp_ge_f32_e64 s[18:19], 0, v5
	v_add_u32_e32 v5, 1, v3
	s_nop 0
	v_cndmask_b32_e64 v4, v3, v4, s[18:19]
	v_fma_f32 v3, -v5, v3, v2
	v_cmp_lt_f32_e64 s[18:19], 0, v3
	s_nop 1
	v_cndmask_b32_e64 v3, v4, v5, s[18:19]
	v_mul_f32_e32 v4, 0x37800000, v3
	v_cndmask_b32_e32 v3, v3, v4, vcc
	v_mov_b32_e32 v4, 0x260
	v_cmp_class_f32_e32 vcc, v2, v4
	s_nop 1
	v_cndmask_b32_e32 v2, v3, v2, vcc
	s_nop 1
	v_add_f32_dpp v3, v2, v2 quad_perm:[1,0,3,2] row_mask:0xf bank_mask:0xf
	s_nop 1
	v_add_f32_dpp v4, v3, v3 quad_perm:[2,3,0,1] row_mask:0xf bank_mask:0xf
	s_nop 1
	v_add_f32_dpp v5, v4, v4 row_half_mirror row_mask:0xf bank_mask:0xf
	s_nop 1
	v_add_f32_dpp v6, v5, v5 row_mirror row_mask:0xf bank_mask:0xf
	s_nop 1
	v_readlane_b32 s12, v6, 0
	v_readlane_b32 s13, v6, 16
	v_readlane_b32 s14, v6, 32
	v_readlane_b32 s15, v6, 48
	s_nop 3
	v_mov_b32_e32 v7, s12
	v_add_f32_e32 v7, s13, v7
	v_mov_b32_e32 v9, s14
	v_add_f32_e32 v9, s15, v9
	v_add_f32_e32 v0, v7, v9
	v_mov_b32_e32 v4, 0
	s_mov_b64 exec, 1
	v_cvt_f64_f32_e32 v[6:7], v0
	v_add_f64 v[8:9], v[6:7], s[4:5]
	global_atomic_add_f64 v[10:11], v4, v[8:9], s[6:7] sc0
	s_waitcnt vmcnt(0)
	v_cmp_le_f64_e32 vcc, s[16:17], v[10:11]
	s_and_saveexec_b64 s[2:3], vcc
	s_cbranch_execz .Lmain_end
	v_add_f64 v[10:11], v[10:11], -s[16:17]
	v_add_f64 v[10:11], v[10:11], v[6:7]
	v_cvt_f32_f64_e32 v0, v[10:11]
	v_mul_f32_e32 v0, 0x38000000, v0
	global_atomic_add_f32 v4, v0, s[10:11]
